# P7: warm the x rows the X1 epilogue reads, one one-dword load per K-loop phase in the last four trips; counted waits widened to vmcnt(9) while it is in flight
# speedup vs baseline: 1.0056x; 1.0005x over previous
.LBB0_757:
	ds_read_b128 v[18:21], v192
	ds_read_b128 v[22:25], v192 offset:1024
	ds_read_b128 v[26:29], v192 offset:2048
	ds_read_b128 v[30:33], v192 offset:3072
	ds_read_b128 v[2:5], v193
	ds_read_b128 v[6:9], v193 offset:1024
	ds_read_b128 v[10:13], v193 offset:2048
	ds_read_b128 v[14:17], v193 offset:3072
	s_add_u32 s48, s46, 0x100
	s_addc_u32 s49, s47, 0
	s_cmp_eq_u32 s72, 12
	s_cselect_b32 s53, s5, s49
	s_cselect_b32 s52, s4, s48
	s_cselect_b32 s51, s43, s41
	s_cselect_b32 s50, s42, s39
	v_lshl_add_u64 v[220:221], s[46:47], 0, v[174:175]
	s_add_i32 m0, s45, 0xc000
	ds_read_b128 v[182:185], v194
	ds_read_b128 v[186:189], v194 offset:1024
	ds_read_b128 v[196:199], v194 offset:2048
	ds_read_b128 v[200:203], v194 offset:3072
	ds_read_b128 v[204:207], v194 offset:4096
	ds_read_b128 v[208:211], v194 offset:5120
	ds_read_b128 v[212:215], v194 offset:6144
	ds_read_b128 v[216:219], v194 offset:7168
	global_load_lds_dwordx4 v[220:221], off
	v_lshl_add_u64 v[220:221], s[46:47], 0, v[176:177]
	s_add_i32 m0, s45, 0xe000
	s_nop 0
	global_load_lds_dwordx4 v[220:221], off
	s_waitcnt vmcnt(9)
	s_cmp_ge_i32 s72, 8
	s_cbranch_scc1 .Lp7pf_w0
	s_waitcnt vmcnt(8)
.Lp7pf_w0:
	s_waitcnt lgkmcnt(0)
	s_barrier
	s_setprio 1
	s_waitcnt lgkmcnt(0)
	v_mfma_scale_f32_16x16x128_f8f6f4 v[158:161], v[18:25], v[182:189], v[158:161], v195, v195 op_sel_hi:[0,0,0]
	v_mfma_scale_f32_16x16x128_f8f6f4 v[154:157], v[26:33], v[182:189], v[154:157], v195, v195 op_sel_hi:[0,0,0]
	v_mfma_scale_f32_16x16x128_f8f6f4 v[146:149], v[18:25], v[196:203], v[146:149], v195, v195 op_sel_hi:[0,0,0]
	v_mfma_scale_f32_16x16x128_f8f6f4 v[142:145], v[26:33], v[196:203], v[142:145], v195, v195 op_sel_hi:[0,0,0]
	v_mfma_scale_f32_16x16x128_f8f6f4 v[130:133], v[18:25], v[204:211], v[130:133], v195, v195 op_sel_hi:[0,0,0]
	v_mfma_scale_f32_16x16x128_f8f6f4 v[126:129], v[26:33], v[204:211], v[126:129], v195, v195 op_sel_hi:[0,0,0]
	v_mfma_scale_f32_16x16x128_f8f6f4 v[114:117], v[18:25], v[212:219], v[114:117], v195, v195 op_sel_hi:[0,0,0]
	v_mfma_scale_f32_16x16x128_f8f6f4 v[110:113], v[26:33], v[212:219], v[110:113], v195, v195 op_sel_hi:[0,0,0]
	s_setprio 0
	s_setprio 1
	v_mfma_scale_f32_16x16x128_f8f6f4 v[150:153], v[2:9], v[182:189], v[150:153], v195, v195 op_sel_hi:[0,0,0]
	v_mfma_scale_f32_16x16x128_f8f6f4 v[138:141], v[10:17], v[182:189], v[138:141], v195, v195 op_sel_hi:[0,0,0]
	v_mfma_scale_f32_16x16x128_f8f6f4 v[134:137], v[2:9], v[196:203], v[134:137], v195, v195 op_sel_hi:[0,0,0]
	v_mfma_scale_f32_16x16x128_f8f6f4 v[122:125], v[10:17], v[196:203], v[122:125], v195, v195 op_sel_hi:[0,0,0]
	v_mfma_scale_f32_16x16x128_f8f6f4 v[118:121], v[2:9], v[204:211], v[118:121], v195, v195 op_sel_hi:[0,0,0]
	v_mfma_scale_f32_16x16x128_f8f6f4 v[106:109], v[10:17], v[204:211], v[106:109], v195, v195 op_sel_hi:[0,0,0]
	v_mfma_scale_f32_16x16x128_f8f6f4 v[98:101], v[2:9], v[212:219], v[98:101], v195, v195 op_sel_hi:[0,0,0]
	v_mfma_scale_f32_16x16x128_f8f6f4 v[90:93], v[10:17], v[212:219], v[90:93], v195, v195 op_sel_hi:[0,0,0]
	s_cmp_ge_i32 s72, 6
	s_cbranch_scc0 .Lp7pf_skip_0
	v_lshlrev_b32_e64 v250, 8, s71
	v_or_b32_e32 v250, s64, v250
	v_lshl_add_u32 v250, v190, 3, v250
	v_lshlrev_b32_e64 v251, 8, s44
	v_add3_u32 v251, v251, s63, v1
	v_lshlrev_b32_e32 v251, 13, v251
	v_lshl_add_u32 v251, v250, 2, v251
	v_mov_b32_e32 v252, s72
	v_add_u32_e32 v252, -6, v252
	v_and_b32_e32 v253, 2, v252
	v_and_b32_e32 v252, 4, v252
	v_lshlrev_b32_e32 v253, 17, v253
	v_lshl_add_u32 v253, v252, 18, v253
	v_add_u32_e32 v251, v251, v253
	global_load_dword v254, v251, s[10:11]
.Lp7pf_skip_0:
	s_setprio 0
	s_barrier
	s_add_i32 s46, s68, s58
	v_lshl_add_u64 v[182:183], s[50:51], 0, v[162:163]
	s_mov_b32 m0, s46
	ds_read_b128 v[196:199], v194 offset:16384
	ds_read_b128 v[200:203], v194 offset:17408
	ds_read_b128 v[204:207], v194 offset:18432
	ds_read_b128 v[208:211], v194 offset:19456
	ds_read_b128 v[212:215], v194 offset:20480
	ds_read_b128 v[216:219], v194 offset:21504
	ds_read_b128 v[220:223], v194 offset:22528
	ds_read_b128 v[224:227], v194 offset:23552
	global_load_lds_dwordx4 v[182:183], off
	s_add_i32 m0, s46, 0x2000
	s_add_u32 s46, s50, 0x40000
	v_lshl_add_u64 v[184:185], s[50:51], 0, v[164:165]
	s_addc_u32 s47, s51, 0
	s_add_i32 s73, s69, s58
	global_load_lds_dwordx4 v[184:185], off
	v_lshl_add_u64 v[186:187], s[46:47], 0, v[162:163]
	s_mov_b32 m0, s73
	v_lshl_add_u64 v[188:189], s[52:53], 0, v[168:169]
	global_load_lds_dwordx4 v[186:187], off
	v_lshl_add_u64 v[186:187], s[46:47], 0, v[164:165]
	s_add_i32 m0, s73, 0x2000
	s_nop 0
	global_load_lds_dwordx4 v[186:187], off
	v_lshl_add_u64 v[186:187], s[52:53], 0, v[166:167]
	s_mov_b32 m0, s45
	s_nop 0
	global_load_lds_dwordx4 v[186:187], off
	s_mov_b32 m0, s59
	s_nop 0
	global_load_lds_dwordx4 v[188:189], off
	s_waitcnt vmcnt(9)
	s_cmp_ge_i32 s72, 6
	s_cbranch_scc1 .Lp7pf_w1
	s_waitcnt vmcnt(8)
.Lp7pf_w1:
	s_waitcnt lgkmcnt(0)
	s_barrier
	s_setprio 1
	s_waitcnt lgkmcnt(0)
	v_mfma_scale_f32_16x16x128_f8f6f4 v[86:89], v[18:25], v[196:203], v[86:89], v195, v195 op_sel_hi:[0,0,0]
	v_mfma_scale_f32_16x16x128_f8f6f4 v[78:81], v[26:33], v[196:203], v[78:81], v195, v195 op_sel_hi:[0,0,0]
	v_mfma_scale_f32_16x16x128_f8f6f4 v[66:69], v[18:25], v[204:211], v[66:69], v195, v195 op_sel_hi:[0,0,0]
	v_mfma_scale_f32_16x16x128_f8f6f4 v[58:61], v[26:33], v[204:211], v[58:61], v195, v195 op_sel_hi:[0,0,0]
	v_mfma_scale_f32_16x16x128_f8f6f4 v[46:49], v[18:25], v[212:219], v[46:49], v195, v195 op_sel_hi:[0,0,0]
	v_mfma_scale_f32_16x16x128_f8f6f4 v[42:45], v[26:33], v[212:219], v[42:45], v195, v195 op_sel_hi:[0,0,0]
	v_mfma_scale_f32_16x16x128_f8f6f4 v[38:41], v[18:25], v[220:227], v[38:41], v195, v195 op_sel_hi:[0,0,0]
	v_mfma_scale_f32_16x16x128_f8f6f4 v[34:37], v[26:33], v[220:227], v[34:37], v195, v195 op_sel_hi:[0,0,0]
	s_setprio 0
	s_setprio 1
	v_mfma_scale_f32_16x16x128_f8f6f4 v[102:105], v[2:9], v[196:203], v[102:105], v195, v195 op_sel_hi:[0,0,0]
	v_mfma_scale_f32_16x16x128_f8f6f4 v[94:97], v[10:17], v[196:203], v[94:97], v195, v195 op_sel_hi:[0,0,0]
	v_mfma_scale_f32_16x16x128_f8f6f4 v[82:85], v[2:9], v[204:211], v[82:85], v195, v195 op_sel_hi:[0,0,0]
	v_mfma_scale_f32_16x16x128_f8f6f4 v[74:77], v[10:17], v[204:211], v[74:77], v195, v195 op_sel_hi:[0,0,0]
	v_mfma_scale_f32_16x16x128_f8f6f4 v[70:73], v[2:9], v[212:219], v[70:73], v195, v195 op_sel_hi:[0,0,0]
	v_mfma_scale_f32_16x16x128_f8f6f4 v[62:65], v[10:17], v[212:219], v[62:65], v195, v195 op_sel_hi:[0,0,0]
	v_mfma_scale_f32_16x16x128_f8f6f4 v[54:57], v[2:9], v[220:227], v[54:57], v195, v195 op_sel_hi:[0,0,0]
	v_mfma_scale_f32_16x16x128_f8f6f4 v[50:53], v[10:17], v[220:227], v[50:53], v195, v195 op_sel_hi:[0,0,0]
	s_cmp_ge_i32 s72, 6
	s_cbranch_scc0 .Lp7pf_skip_1
	v_lshlrev_b32_e64 v250, 8, s71
	v_or_b32_e32 v250, s64, v250
	v_lshl_add_u32 v250, v190, 3, v250
	v_lshlrev_b32_e64 v251, 8, s44
	v_add3_u32 v251, v251, s63, v1
	v_lshlrev_b32_e32 v251, 13, v251
	v_lshl_add_u32 v251, v250, 2, v251
	v_mov_b32_e32 v252, s72
	v_add_u32_e32 v252, -6, v252
	v_and_b32_e32 v253, 2, v252
	v_and_b32_e32 v252, 4, v252
	v_lshlrev_b32_e32 v253, 17, v253
	v_lshl_add_u32 v253, v252, 18, v253
	v_add_u32_e32 v251, v251, v253
	global_load_dword v254, v251, s[10:11] offset:512
.Lp7pf_skip_1:
	s_setprio 0
	s_barrier
	s_add_i32 s46, 0, 0x18000
	s_add_i32 s73, 0, 0x1c000
	v_add_u32_e32 v14, s46, v191
	v_add_u32_e32 v30, s73, v191
	ds_read_b128 v[2:5], v14
	ds_read_b128 v[6:9], v14 offset:1024
	ds_read_b128 v[10:13], v14 offset:2048
	ds_read_b128 v[14:17], v14 offset:3072
	ds_read_b128 v[18:21], v30
	ds_read_b128 v[22:25], v30 offset:1024
	ds_read_b128 v[26:29], v30 offset:2048
	ds_read_b128 v[30:33], v30 offset:3072
	s_mov_b32 m0, s60
	v_lshl_add_u64 v[228:229], s[52:53], 0, v[170:171]
	ds_read_b128 v[196:199], v194 offset:32768
	ds_read_b128 v[200:203], v194 offset:33792
	ds_read_b128 v[204:207], v194 offset:34816
	ds_read_b128 v[208:211], v194 offset:35840
	ds_read_b128 v[212:215], v194 offset:36864
	ds_read_b128 v[216:219], v194 offset:37888
	ds_read_b128 v[220:223], v194 offset:38912
	ds_read_b128 v[224:227], v194 offset:39936
	global_load_lds_dwordx4 v[228:229], off
	v_lshl_add_u64 v[228:229], s[52:53], 0, v[172:173]
	s_mov_b32 m0, s61
	s_nop 0
	global_load_lds_dwordx4 v[228:229], off
	s_waitcnt vmcnt(9)
	s_cmp_ge_i32 s72, 6
	s_cbranch_scc1 .Lp7pf_w2
	s_waitcnt vmcnt(8)
.Lp7pf_w2:
	s_waitcnt lgkmcnt(0)
	s_barrier
	s_setprio 1
	s_waitcnt lgkmcnt(0)
	v_mfma_scale_f32_16x16x128_f8f6f4 v[158:161], v[2:9], v[196:203], v[158:161], v195, v195 op_sel_hi:[0,0,0]
	v_mfma_scale_f32_16x16x128_f8f6f4 v[154:157], v[10:17], v[196:203], v[154:157], v195, v195 op_sel_hi:[0,0,0]
	v_mfma_scale_f32_16x16x128_f8f6f4 v[146:149], v[2:9], v[204:211], v[146:149], v195, v195 op_sel_hi:[0,0,0]
	v_mfma_scale_f32_16x16x128_f8f6f4 v[142:145], v[10:17], v[204:211], v[142:145], v195, v195 op_sel_hi:[0,0,0]
	v_mfma_scale_f32_16x16x128_f8f6f4 v[130:133], v[2:9], v[212:219], v[130:133], v195, v195 op_sel_hi:[0,0,0]
	v_mfma_scale_f32_16x16x128_f8f6f4 v[126:129], v[10:17], v[212:219], v[126:129], v195, v195 op_sel_hi:[0,0,0]
	v_mfma_scale_f32_16x16x128_f8f6f4 v[114:117], v[2:9], v[220:227], v[114:117], v195, v195 op_sel_hi:[0,0,0]
	v_mfma_scale_f32_16x16x128_f8f6f4 v[110:113], v[10:17], v[220:227], v[110:113], v195, v195 op_sel_hi:[0,0,0]
	s_setprio 0
	s_setprio 1
	v_mfma_scale_f32_16x16x128_f8f6f4 v[150:153], v[18:25], v[196:203], v[150:153], v195, v195 op_sel_hi:[0,0,0]
	v_mfma_scale_f32_16x16x128_f8f6f4 v[138:141], v[26:33], v[196:203], v[138:141], v195, v195 op_sel_hi:[0,0,0]
	v_mfma_scale_f32_16x16x128_f8f6f4 v[134:137], v[18:25], v[204:211], v[134:137], v195, v195 op_sel_hi:[0,0,0]
	v_mfma_scale_f32_16x16x128_f8f6f4 v[122:125], v[26:33], v[204:211], v[122:125], v195, v195 op_sel_hi:[0,0,0]
	v_mfma_scale_f32_16x16x128_f8f6f4 v[118:121], v[18:25], v[212:219], v[118:121], v195, v195 op_sel_hi:[0,0,0]
	v_mfma_scale_f32_16x16x128_f8f6f4 v[106:109], v[26:33], v[212:219], v[106:109], v195, v195 op_sel_hi:[0,0,0]
	v_mfma_scale_f32_16x16x128_f8f6f4 v[98:101], v[18:25], v[220:227], v[98:101], v195, v195 op_sel_hi:[0,0,0]
	v_mfma_scale_f32_16x16x128_f8f6f4 v[90:93], v[26:33], v[220:227], v[90:93], v195, v195 op_sel_hi:[0,0,0]
	s_cmp_ge_i32 s72, 6
	s_cbranch_scc0 .Lp7pf_skip_2
	v_lshlrev_b32_e64 v250, 8, s71
	v_or_b32_e32 v250, s64, v250
	v_lshl_add_u32 v250, v190, 3, v250
	v_lshlrev_b32_e64 v251, 8, s44
	v_add3_u32 v251, v251, s63, v1
	v_lshlrev_b32_e32 v251, 13, v251
	v_lshl_add_u32 v251, v250, 2, v251
	v_mov_b32_e32 v252, s72
	v_add_u32_e32 v252, -6, v252
	v_and_b32_e32 v253, 2, v252
	v_and_b32_e32 v252, 4, v252
	v_lshlrev_b32_e32 v253, 17, v253
	v_lshl_add_u32 v253, v252, 18, v253
	v_add_u32_e32 v251, v251, v253
	v_add_u32_e32 v251, 0x20000, v251
	global_load_dword v254, v251, s[10:11]
.Lp7pf_skip_2:
	s_setprio 0
	s_barrier
	s_add_i32 s46, s46, s58
	v_lshl_add_u64 v[182:183], v[182:183], 0, s[16:17]
	s_mov_b32 m0, s46
	ds_read_b128 v[196:199], v194 offset:49152
	ds_read_b128 v[200:203], v194 offset:50176
	ds_read_b128 v[204:207], v194 offset:51200
	ds_read_b128 v[208:211], v194 offset:52224
	ds_read_b128 v[212:215], v194 offset:53248
	ds_read_b128 v[216:219], v194 offset:54272
	ds_read_b128 v[220:223], v194 offset:55296
	ds_read_b128 v[224:227], v194 offset:56320
	global_load_lds_dwordx4 v[182:183], off
	s_add_i32 m0, s46, 0x2000
	s_add_u32 s46, s50, 0x40080
	v_lshl_add_u64 v[182:183], v[184:185], 0, s[16:17]
	s_addc_u32 s47, s51, 0
	s_add_i32 s50, s73, s58
	global_load_lds_dwordx4 v[182:183], off
	v_lshl_add_u64 v[182:183], s[46:47], 0, v[162:163]
	s_mov_b32 m0, s50
	s_nop 0
	global_load_lds_dwordx4 v[182:183], off
	v_lshl_add_u64 v[182:183], s[46:47], 0, v[164:165]
	s_add_i32 m0, s50, 0x2000
	s_nop 0
	global_load_lds_dwordx4 v[182:183], off
	v_lshl_add_u64 v[182:183], v[186:187], 0, s[16:17]
	s_mov_b32 m0, s65
	s_nop 0
	global_load_lds_dwordx4 v[182:183], off
	v_lshl_add_u64 v[182:183], v[188:189], 0, s[16:17]
	s_mov_b32 m0, s66
	s_nop 0
	global_load_lds_dwordx4 v[182:183], off
	s_waitcnt vmcnt(9)
	s_cmp_ge_i32 s72, 6
	s_cbranch_scc1 .Lp7pf_w3
	s_waitcnt vmcnt(8)
.Lp7pf_w3:
	s_waitcnt lgkmcnt(0)
	s_barrier
	s_setprio 1
	s_waitcnt lgkmcnt(0)
	v_mfma_scale_f32_16x16x128_f8f6f4 v[86:89], v[2:9], v[196:203], v[86:89], v195, v195 op_sel_hi:[0,0,0]
	v_mfma_scale_f32_16x16x128_f8f6f4 v[78:81], v[10:17], v[196:203], v[78:81], v195, v195 op_sel_hi:[0,0,0]
	v_mfma_scale_f32_16x16x128_f8f6f4 v[66:69], v[2:9], v[204:211], v[66:69], v195, v195 op_sel_hi:[0,0,0]
	v_mfma_scale_f32_16x16x128_f8f6f4 v[58:61], v[10:17], v[204:211], v[58:61], v195, v195 op_sel_hi:[0,0,0]
	v_mfma_scale_f32_16x16x128_f8f6f4 v[46:49], v[2:9], v[212:219], v[46:49], v195, v195 op_sel_hi:[0,0,0]
	v_mfma_scale_f32_16x16x128_f8f6f4 v[42:45], v[10:17], v[212:219], v[42:45], v195, v195 op_sel_hi:[0,0,0]
	v_mfma_scale_f32_16x16x128_f8f6f4 v[38:41], v[2:9], v[220:227], v[38:41], v195, v195 op_sel_hi:[0,0,0]
	v_mfma_scale_f32_16x16x128_f8f6f4 v[34:37], v[10:17], v[220:227], v[34:37], v195, v195 op_sel_hi:[0,0,0]
	s_setprio 0
	s_setprio 1
	v_mfma_scale_f32_16x16x128_f8f6f4 v[102:105], v[18:25], v[196:203], v[102:105], v195, v195 op_sel_hi:[0,0,0]
	v_mfma_scale_f32_16x16x128_f8f6f4 v[94:97], v[26:33], v[196:203], v[94:97], v195, v195 op_sel_hi:[0,0,0]
	v_mfma_scale_f32_16x16x128_f8f6f4 v[82:85], v[18:25], v[204:211], v[82:85], v195, v195 op_sel_hi:[0,0,0]
	v_mfma_scale_f32_16x16x128_f8f6f4 v[74:77], v[26:33], v[204:211], v[74:77], v195, v195 op_sel_hi:[0,0,0]
	v_mfma_scale_f32_16x16x128_f8f6f4 v[70:73], v[18:25], v[212:219], v[70:73], v195, v195 op_sel_hi:[0,0,0]
	v_mfma_scale_f32_16x16x128_f8f6f4 v[62:65], v[26:33], v[212:219], v[62:65], v195, v195 op_sel_hi:[0,0,0]
	v_mfma_scale_f32_16x16x128_f8f6f4 v[54:57], v[18:25], v[220:227], v[54:57], v195, v195 op_sel_hi:[0,0,0]
	v_mfma_scale_f32_16x16x128_f8f6f4 v[50:53], v[26:33], v[220:227], v[50:53], v195, v195 op_sel_hi:[0,0,0]
	s_cmp_ge_i32 s72, 6
	s_cbranch_scc0 .Lp7pf_skip_3
	v_lshlrev_b32_e64 v250, 8, s71
	v_or_b32_e32 v250, s64, v250
	v_lshl_add_u32 v250, v190, 3, v250
	v_lshlrev_b32_e64 v251, 8, s44
	v_add3_u32 v251, v251, s63, v1
	v_lshlrev_b32_e32 v251, 13, v251
	v_lshl_add_u32 v251, v250, 2, v251
	v_mov_b32_e32 v252, s72
	v_add_u32_e32 v252, -6, v252
	v_and_b32_e32 v253, 2, v252
	v_and_b32_e32 v252, 4, v252
	v_lshlrev_b32_e32 v253, 17, v253
	v_lshl_add_u32 v253, v252, 18, v253
	v_add_u32_e32 v251, v251, v253
	v_add_u32_e32 v251, 0x20000, v251
	global_load_dword v254, v251, s[10:11] offset:512
.Lp7pf_skip_3:
	s_setprio 0
	s_barrier
	s_add_i32 s72, s72, 2
	s_add_u32 s39, s39, 0x100
	s_addc_u32 s41, s41, 0
	s_cmp_gt_u32 s72, 13
	s_mov_b64 s[46:47], s[48:49]
	s_cbranch_scc0 .LBB0_757
	s_and_b64 vcc, exec, s[18:19]
	s_cbranch_vccz .LBB0_760
	s_barrier
